# rtab pre-pass: all loads in flight; GEMM prologues issue both K-tiles DMAs before the first wait; K-loop prio trims
# speedup vs baseline: 1.0017x; 1.0017x over previous
.LBB0_252:
	s_andn2_b64 vcc, exec, s[0:1]
	s_cbranch_vccnz .LBB0_373
	v_readlane_b32 s0, v254, 48
	v_readlane_b32 s1, v254, 49
	s_andn2_b64 vcc, exec, s[0:1]
	v_readlane_b32 s0, v254, 6
	s_mov_b32 s10, s79
	v_mov_b32_e32 v4, v0
	v_readlane_b32 s1, v254, 7
	s_load_dword s22, s[0:1], 0x0
	v_readlane_b32 s0, v254, 37
	s_movk_i32 s1, 0x800
	v_cmp_ne_u32_e64 s[4:5], 1, v206
	s_ashr_i32 s11, s10, 31
	s_and_b32 s0, s0, -8
	v_cmp_gt_i32_e32 vcc, s1, v4
	s_and_saveexec_b64 s[6:7], vcc
	s_cbranch_execz .LBB0_256
	s_ashr_i32 s1, s0, 31
	s_lshl_b64 s[8:9], s[0:1], 14
	v_readlane_b32 s1, v254, 50
	v_readlane_b32 s13, v254, 39
	v_ashrrev_i32_e32 v5, 31, v4
	v_lshl_add_u32 v2, v4, 2, s1
	v_readlane_b32 s1, v254, 38
	s_add_u32 s1, s1, s10
	s_addc_u32 s13, s13, s11
	s_add_u32 s8, s1, s8
	v_add_u32_e32 v1, 0xfffffe00, v4
	v_lshlrev_b64 v[4:5], 6, v[4:5]
	s_addc_u32 s9, s13, s9
	v_lshl_add_u64 v[4:5], s[8:9], 0, v[4:5]
	s_mov_b64 s[8:9], 0
	s_mov_b64 s[14:15], 0x8000
	global_load_dwordx4 v[6:9], v[4:5], off offset:16
	global_load_dwordx4 v[10:13], v[4:5], off
	global_load_dwordx4 v[14:17], v[4:5], off offset:-16
	global_load_dwordx4 v[18:21], v[4:5], off offset:-32
	v_lshl_add_u64 v[24:25], v[4:5], 0, s[14:15]
	global_load_dwordx4 v[26:29], v[24:25], off offset:16
	global_load_dwordx4 v[30:33], v[24:25], off
	global_load_dwordx4 v[34:37], v[24:25], off offset:-16
	global_load_dwordx4 v[38:41], v[24:25], off offset:-32
	v_lshl_add_u64 v[42:43], v[24:25], 0, s[14:15]
	global_load_dwordx4 v[44:47], v[42:43], off offset:16
	global_load_dwordx4 v[48:51], v[42:43], off
	global_load_dwordx4 v[52:55], v[42:43], off offset:-16
	global_load_dwordx4 v[56:59], v[42:43], off offset:-32
	v_lshl_add_u64 v[60:61], v[42:43], 0, s[14:15]
	global_load_dwordx4 v[62:65], v[60:61], off offset:16
	global_load_dwordx4 v[66:69], v[60:61], off
	global_load_dwordx4 v[70:73], v[60:61], off offset:-16
	global_load_dwordx4 v[74:77], v[60:61], off offset:-32
	s_waitcnt vmcnt(12)
	v_add_f32_e32 v10, v10, v11
	v_add_f32_e32 v12, v12, v13
	v_mov_b32_e32 v22, v19
	v_mov_b32_e32 v23, v20
	v_mov_b32_e32 v19, v21
	v_mov_b32_e32 v20, v15
	v_mov_b32_e32 v21, v16
	v_mov_b32_e32 v15, v17
	v_pk_add_f32 v[18:19], v[22:23], v[18:19]
	v_pk_add_f32 v[14:15], v[20:21], v[14:15]
	v_pk_add_f32 v[18:19], v[18:19], v[18:19] op_sel:[0,1] op_sel_hi:[1,0]
	v_pk_add_f32 v[14:15], v[14:15], v[14:15] op_sel:[0,1] op_sel_hi:[1,0]
	v_mov_b32_e32 v19, v6
	v_mov_b32_e32 v15, v7
	v_mov_b32_e32 v11, v8
	v_mov_b32_e32 v13, v9
	v_pk_add_f32 v[6:7], v[18:19], v[14:15]
	v_pk_add_f32 v[8:9], v[10:11], v[12:13]
	s_nop 0
	v_pk_add_f32 v[6:7], v[6:7], v[8:9]
	s_nop 0
	v_add_f32_e32 v6, v6, v7
	v_fmamk_f32 v6, v6, 0x39800000, v207
	v_cmp_gt_f32_e32 vcc, s43, v6
	v_mul_f32_e32 v7, 0x4b800000, v6
	s_nop 0
	v_cndmask_b32_e32 v6, v6, v7, vcc
	v_rsq_f32_e32 v6, v6
	s_nop 0
	v_mul_f32_e32 v7, 0x45800000, v6
	v_cndmask_b32_e32 v6, v6, v7, vcc
	ds_write_b32 v2, v6
	v_add_u32_e32 v2, 0x800, v2
	s_waitcnt vmcnt(8)
	v_mov_b32_e32 v6, v26
	v_mov_b32_e32 v7, v27
	v_mov_b32_e32 v8, v28
	v_mov_b32_e32 v9, v29
	v_mov_b32_e32 v10, v30
	v_mov_b32_e32 v11, v31
	v_mov_b32_e32 v12, v32
	v_mov_b32_e32 v13, v33
	v_mov_b32_e32 v14, v34
	v_mov_b32_e32 v15, v35
	v_mov_b32_e32 v16, v36
	v_mov_b32_e32 v17, v37
	v_mov_b32_e32 v18, v38
	v_mov_b32_e32 v19, v39
	v_mov_b32_e32 v20, v40
	v_mov_b32_e32 v21, v41
	v_add_f32_e32 v10, v10, v11
	v_add_f32_e32 v12, v12, v13
	v_mov_b32_e32 v22, v19
	v_mov_b32_e32 v23, v20
	v_mov_b32_e32 v19, v21
	v_mov_b32_e32 v20, v15
	v_mov_b32_e32 v21, v16
	v_mov_b32_e32 v15, v17
	v_pk_add_f32 v[18:19], v[22:23], v[18:19]
	v_pk_add_f32 v[14:15], v[20:21], v[14:15]
	v_pk_add_f32 v[18:19], v[18:19], v[18:19] op_sel:[0,1] op_sel_hi:[1,0]
	v_pk_add_f32 v[14:15], v[14:15], v[14:15] op_sel:[0,1] op_sel_hi:[1,0]
	v_mov_b32_e32 v19, v6
	v_mov_b32_e32 v15, v7
	v_mov_b32_e32 v11, v8
	v_mov_b32_e32 v13, v9
	v_pk_add_f32 v[6:7], v[18:19], v[14:15]
	v_pk_add_f32 v[8:9], v[10:11], v[12:13]
	s_nop 0
	v_pk_add_f32 v[6:7], v[6:7], v[8:9]
	s_nop 0
	v_add_f32_e32 v6, v6, v7
	v_fmamk_f32 v6, v6, 0x39800000, v207
	v_cmp_gt_f32_e32 vcc, s43, v6
	v_mul_f32_e32 v7, 0x4b800000, v6
	s_nop 0
	v_cndmask_b32_e32 v6, v6, v7, vcc
	v_rsq_f32_e32 v6, v6
	s_nop 0
	v_mul_f32_e32 v7, 0x45800000, v6
	v_cndmask_b32_e32 v6, v6, v7, vcc
	ds_write_b32 v2, v6
	v_add_u32_e32 v2, 0x800, v2
	s_waitcnt vmcnt(4)
	v_mov_b32_e32 v6, v44
	v_mov_b32_e32 v7, v45
	v_mov_b32_e32 v8, v46
	v_mov_b32_e32 v9, v47
	v_mov_b32_e32 v10, v48
	v_mov_b32_e32 v11, v49
	v_mov_b32_e32 v12, v50
	v_mov_b32_e32 v13, v51
	v_mov_b32_e32 v14, v52
	v_mov_b32_e32 v15, v53
	v_mov_b32_e32 v16, v54
	v_mov_b32_e32 v17, v55
	v_mov_b32_e32 v18, v56
	v_mov_b32_e32 v19, v57
	v_mov_b32_e32 v20, v58
	v_mov_b32_e32 v21, v59
	v_add_f32_e32 v10, v10, v11
	v_add_f32_e32 v12, v12, v13
	v_mov_b32_e32 v22, v19
	v_mov_b32_e32 v23, v20
	v_mov_b32_e32 v19, v21
	v_mov_b32_e32 v20, v15
	v_mov_b32_e32 v21, v16
	v_mov_b32_e32 v15, v17
	v_pk_add_f32 v[18:19], v[22:23], v[18:19]
	v_pk_add_f32 v[14:15], v[20:21], v[14:15]
	v_pk_add_f32 v[18:19], v[18:19], v[18:19] op_sel:[0,1] op_sel_hi:[1,0]
	v_pk_add_f32 v[14:15], v[14:15], v[14:15] op_sel:[0,1] op_sel_hi:[1,0]
	v_mov_b32_e32 v19, v6
	v_mov_b32_e32 v15, v7
	v_mov_b32_e32 v11, v8
	v_mov_b32_e32 v13, v9
	v_pk_add_f32 v[6:7], v[18:19], v[14:15]
	v_pk_add_f32 v[8:9], v[10:11], v[12:13]
	s_nop 0
	v_pk_add_f32 v[6:7], v[6:7], v[8:9]
	s_nop 0
	v_add_f32_e32 v6, v6, v7
	v_fmamk_f32 v6, v6, 0x39800000, v207
	v_cmp_gt_f32_e32 vcc, s43, v6
	v_mul_f32_e32 v7, 0x4b800000, v6
	s_nop 0
	v_cndmask_b32_e32 v6, v6, v7, vcc
	v_rsq_f32_e32 v6, v6
	s_nop 0
	v_mul_f32_e32 v7, 0x45800000, v6
	v_cndmask_b32_e32 v6, v6, v7, vcc
	ds_write_b32 v2, v6
	v_add_u32_e32 v2, 0x800, v2
	s_waitcnt vmcnt(0)
	v_mov_b32_e32 v6, v62
	v_mov_b32_e32 v7, v63
	v_mov_b32_e32 v8, v64
	v_mov_b32_e32 v9, v65
	v_mov_b32_e32 v10, v66
	v_mov_b32_e32 v11, v67
	v_mov_b32_e32 v12, v68
	v_mov_b32_e32 v13, v69
	v_mov_b32_e32 v14, v70
	v_mov_b32_e32 v15, v71
	v_mov_b32_e32 v16, v72
	v_mov_b32_e32 v17, v73
	v_mov_b32_e32 v18, v74
	v_mov_b32_e32 v19, v75
	v_mov_b32_e32 v20, v76
	v_mov_b32_e32 v21, v77
	v_add_f32_e32 v10, v10, v11
	v_add_f32_e32 v12, v12, v13
	v_mov_b32_e32 v22, v19
	v_mov_b32_e32 v23, v20
	v_mov_b32_e32 v19, v21
	v_mov_b32_e32 v20, v15
	v_mov_b32_e32 v21, v16
	v_mov_b32_e32 v15, v17
	v_pk_add_f32 v[18:19], v[22:23], v[18:19]
	v_pk_add_f32 v[14:15], v[20:21], v[14:15]
	v_pk_add_f32 v[18:19], v[18:19], v[18:19] op_sel:[0,1] op_sel_hi:[1,0]
	v_pk_add_f32 v[14:15], v[14:15], v[14:15] op_sel:[0,1] op_sel_hi:[1,0]
	v_mov_b32_e32 v19, v6
	v_mov_b32_e32 v15, v7
	v_mov_b32_e32 v11, v8
	v_mov_b32_e32 v13, v9
	v_pk_add_f32 v[6:7], v[18:19], v[14:15]
	v_pk_add_f32 v[8:9], v[10:11], v[12:13]
	s_nop 0
	v_pk_add_f32 v[6:7], v[6:7], v[8:9]
	s_nop 0
	v_add_f32_e32 v6, v6, v7
	v_fmamk_f32 v6, v6, 0x39800000, v207
	v_cmp_gt_f32_e32 vcc, s43, v6
	v_mul_f32_e32 v7, 0x4b800000, v6
	s_nop 0
	v_cndmask_b32_e32 v6, v6, v7, vcc
	v_rsq_f32_e32 v6, v6
	s_nop 0
	v_mul_f32_e32 v7, 0x45800000, v6
	v_cndmask_b32_e32 v6, v6, v7, vcc
	ds_write_b32 v2, v6

.LBB0_259:
	s_add_u32 s10, s13, 0x2f800000
	s_addc_u32 s11, s17, 0
	s_add_u32 s14, s13, 0x800000
	s_addc_u32 s15, s17, 0
	s_and_b32 s21, s16, 3
	s_lshl_b32 s55, s4, 6
	s_lshl_b32 s23, s4, 13
	s_lshl_b32 s61, s21, 5
	s_lshl_b32 s28, s21, 12
	s_add_u32 s16, s13, 0x200000
	s_addc_u32 s17, s17, 0
	s_add_i32 m0, s46, 0x18000
	v_lshl_add_u64 v[10:11], v[10:11], 0, s[86:87]
	global_load_lds_dwordx4 v[10:11], off
	v_lshl_add_u64 v[8:9], v[8:9], 0, s[86:87]
	s_add_i32 m0, s46, 0x1a000
	s_add_i32 s78, s46, 0x8000
	s_add_i32 s85, s46, 0xa000
	global_load_lds_dwordx4 v[8:9], off
	v_lshl_add_u64 v[4:5], v[4:5], 0, s[86:87]
	s_mov_b32 m0, s78
	s_add_u32 s26, s24, 0x100080
	global_load_lds_dwordx4 v[4:5], off
	v_lshl_add_u64 v[4:5], v[6:7], 0, s[86:87]
	s_mov_b32 m0, s85
	s_addc_u32 s27, s25, 0
	global_load_lds_dwordx4 v[4:5], off
	s_add_i32 m0, s46, 0x1c000
	v_lshl_add_u64 v[4:5], s[26:27], 0, v[2:3]
	global_load_lds_dwordx4 v[4:5], off
	v_lshl_add_u64 v[4:5], s[26:27], 0, v[168:169]
	s_add_i32 m0, s46, 0x1e000
	v_bfe_u32 v157, v12, 4, 2
	global_load_lds_dwordx4 v[4:5], off
	s_waitcnt vmcnt(8)
	s_barrier
	v_and_b32_e32 v1, 15, v12
	v_lshlrev_b32_e32 v4, 4, v157
	v_lshlrev_b32_e32 v5, 2, v12
	v_lshl_or_b32 v4, v1, 6, v4
	v_and_b32_e32 v5, 32, v5
	v_bitop3_b32 v6, v4, s23, v5 bitop3:0xde
	v_bitop3_b32 v163, v4, s28, v5 bitop3:0xde
	v_lshlrev_b32_e32 v4, 16, v17
	v_and_b32_e32 v4, 0xfffe0000, v4
	v_lshl_add_u32 v4, v16, 13, v4
	v_and_b32_e32 v5, 1, v17
	v_lshl_or_b32 v4, v5, 6, v4
	s_cmpk_lt_u32 s5, 0x100
	v_lshl_add_u32 v174, v18, 1, v4
	v_lshlrev_b32_e32 v4, 16, v13
	s_cselect_b64 s[30:31], -1, 0
	s_cmp_eq_u32 s21, 0
	v_and_b32_e32 v4, 0xfffe0000, v4
	s_waitcnt vmcnt(6)
	s_cselect_b64 s[52:53], -1, 0
	s_lshl_b32 s4, s4, 8
	v_lshl_add_u32 v4, v14, 13, v4
	v_and_b32_e32 v5, 1, v13
	s_add_i32 s88, s4, 0
	v_lshl_or_b32 v4, v5, 6, v4
	v_readlane_b32 s4, v254, 25
	s_mov_b32 s93, 0
	s_ashr_i32 s23, s22, 31
	s_add_i32 s88, s88, 0x20400
	v_mov_b32_e32 v175, v3
	v_lshl_add_u32 v176, v15, 1, v4
	v_mov_b32_e32 v177, v3
	v_add_u32_e32 v184, 0, v6
	v_readlane_b32 s92, v254, 23
	s_mov_b32 s35, s4
	s_barrier
	v_readlane_b32 s5, v254, 26
	s_branch .LBB0_262

.LBB0_721:
	v_bfe_u32 v1, v18, 4, 2
	v_and_b32_e32 v142, 15, v18
	v_lshlrev_b32_e32 v19, 4, v1
	v_lshlrev_b32_e32 v18, 2, v18
	s_and_b32 s44, s21, 3
	v_lshl_or_b32 v19, v142, 6, v19
	s_lshl_b32 s21, s25, 13
	v_and_b32_e32 v18, 32, v18
	s_add_i32 m0, s5, 0x18000
	v_lshl_add_u64 v[10:11], v[10:11], 0, s[86:87]
	s_lshl_b32 s40, s25, 6
	v_bitop3_b32 v20, v19, s21, v18 bitop3:0xde
	s_lshl_b32 s21, s44, 12
	global_load_lds_dwordx4 v[10:11], off
	v_lshl_add_u64 v[8:9], v[8:9], 0, s[86:87]
	s_add_i32 m0, s5, 0x1a000
	s_add_i32 s46, s5, 0x8000
	s_add_i32 s50, s5, 0xa000
	global_load_lds_dwordx4 v[8:9], off
	v_lshl_add_u64 v[6:7], v[6:7], 0, s[86:87]
	s_mov_b32 m0, s46
	s_add_u32 s26, s6, 0x100080
	global_load_lds_dwordx4 v[6:7], off
	v_lshl_add_u64 v[4:5], v[4:5], 0, s[86:87]
	s_mov_b32 m0, s50
	s_addc_u32 s27, s7, 0
	global_load_lds_dwordx4 v[4:5], off
	s_add_i32 m0, s5, 0x1c000
	v_lshl_add_u64 v[4:5], s[26:27], 0, v[2:3]
	global_load_lds_dwordx4 v[4:5], off
	v_lshl_add_u64 v[4:5], s[26:27], 0, v[136:137]
	s_add_i32 m0, s5, 0x1e000
	v_bitop3_b32 v143, v19, s21, v18 bitop3:0xde
	global_load_lds_dwordx4 v[4:5], off
	s_waitcnt vmcnt(8)
	s_barrier
	s_add_u32 s21, s24, s30
	s_addc_u32 s25, 0, s13
	v_lshlrev_b32_e32 v4, 16, v12
	s_add_u32 s51, s36, s21
	v_and_b32_e32 v4, 0xfffe0000, v4
	s_addc_u32 s52, s37, s25
	v_lshl_add_u32 v4, v13, 13, v4
	v_and_b32_e32 v5, 1, v12
	v_readlane_b32 s24, v254, 40
	v_lshl_or_b32 v4, v5, 6, v4
	s_add_u32 s24, s24, s21
	v_readlane_b32 s21, v254, 41
	v_lshl_add_u32 v4, v14, 1, v4
	v_mov_b32_e32 v5, v3
	s_addc_u32 s25, s21, s25
	v_lshl_add_u64 v[138:139], s[24:25], 0, v[4:5]
	v_lshlrev_b32_e32 v4, 16, v15
	v_and_b32_e32 v4, 0xfffe0000, v4
	v_lshl_add_u32 v4, v16, 13, v4
	v_and_b32_e32 v5, 1, v15
	v_lshl_or_b32 v4, v5, 6, v4
	s_add_u32 s10, s10, s30
	s_waitcnt vmcnt(6)
	v_lshl_add_u32 v4, v17, 1, v4
	v_mov_b32_e32 v5, v3
	s_addc_u32 s11, s11, s13
	v_readlane_b32 s13, v254, 42
	v_lshl_add_u64 v[140:141], s[24:25], 0, v[4:5]
	s_add_u32 s13, s13, s10
	v_readlane_b32 s10, v254, 43
	v_mov_b32_e32 v4, 0
	s_addc_u32 s21, s10, s11
	s_mov_b32 s53, -2
	s_mov_b64 s[10:11], 0
	v_add_u32_e32 v144, 0, v20
	v_mov_b32_e32 v5, v4
	v_mov_b32_e32 v6, v4
	v_mov_b32_e32 v7, v4
	v_mov_b32_e32 v8, v4
	v_mov_b32_e32 v9, v4
	v_mov_b32_e32 v10, v4
	v_mov_b32_e32 v11, v4
	v_mov_b32_e32 v16, v4
	v_mov_b32_e32 v17, v4
	v_mov_b32_e32 v18, v4
	v_mov_b32_e32 v19, v4
	v_mov_b32_e32 v24, v4
	v_mov_b32_e32 v25, v4
	v_mov_b32_e32 v26, v4
	v_mov_b32_e32 v27, v4
	v_mov_b32_e32 v32, v4
	v_mov_b32_e32 v33, v4
	v_mov_b32_e32 v34, v4
	v_mov_b32_e32 v35, v4
	v_mov_b32_e32 v40, v4
	v_mov_b32_e32 v41, v4
	v_mov_b32_e32 v42, v4
	v_mov_b32_e32 v43, v4
	v_mov_b32_e32 v48, v4
	v_mov_b32_e32 v49, v4
	v_mov_b32_e32 v50, v4
	v_mov_b32_e32 v51, v4
	v_mov_b32_e32 v56, v4
	v_mov_b32_e32 v57, v4
	v_mov_b32_e32 v58, v4
	v_mov_b32_e32 v59, v4
	v_mov_b32_e32 v12, v4
	v_mov_b32_e32 v13, v4
	v_mov_b32_e32 v14, v4
	v_mov_b32_e32 v15, v4
	v_mov_b32_e32 v20, v4
	v_mov_b32_e32 v21, v4
	v_mov_b32_e32 v22, v4
	v_mov_b32_e32 v23, v4
	v_mov_b32_e32 v28, v4
	v_mov_b32_e32 v29, v4
	v_mov_b32_e32 v30, v4
	v_mov_b32_e32 v31, v4
	v_mov_b32_e32 v36, v4
	v_mov_b32_e32 v37, v4
	v_mov_b32_e32 v38, v4
	v_mov_b32_e32 v39, v4
	v_mov_b32_e32 v44, v4
	v_mov_b32_e32 v45, v4
	v_mov_b32_e32 v46, v4
	v_mov_b32_e32 v47, v4
	v_mov_b32_e32 v52, v4
	v_mov_b32_e32 v53, v4
	v_mov_b32_e32 v54, v4
	v_mov_b32_e32 v55, v4
	v_mov_b32_e32 v60, v4
	v_mov_b32_e32 v61, v4
	v_mov_b32_e32 v62, v4
	v_mov_b32_e32 v63, v4
	v_mov_b32_e32 v64, v4
	v_mov_b32_e32 v65, v4
	v_mov_b32_e32 v66, v4
	v_mov_b32_e32 v67, v4
	v_mov_b32_e32 v68, v4
	v_mov_b32_e32 v69, v4
	v_mov_b32_e32 v70, v4
	v_mov_b32_e32 v71, v4
	v_mov_b32_e32 v72, v4
	v_mov_b32_e32 v73, v4
	v_mov_b32_e32 v74, v4
	v_mov_b32_e32 v75, v4
	v_mov_b32_e32 v80, v4
	v_mov_b32_e32 v81, v4
	v_mov_b32_e32 v82, v4
	v_mov_b32_e32 v83, v4
	v_mov_b32_e32 v88, v4
	v_mov_b32_e32 v89, v4
	v_mov_b32_e32 v90, v4
	v_mov_b32_e32 v91, v4
	v_mov_b32_e32 v96, v4
	v_mov_b32_e32 v97, v4
	v_mov_b32_e32 v98, v4
	v_mov_b32_e32 v99, v4
	v_mov_b32_e32 v104, v4
	v_mov_b32_e32 v105, v4
	v_mov_b32_e32 v106, v4
	v_mov_b32_e32 v107, v4
	v_mov_b32_e32 v112, v4
	v_mov_b32_e32 v113, v4
	v_mov_b32_e32 v114, v4
	v_mov_b32_e32 v115, v4
	v_mov_b32_e32 v120, v4
	v_mov_b32_e32 v121, v4
	v_mov_b32_e32 v122, v4
	v_mov_b32_e32 v123, v4
	v_mov_b32_e32 v76, v4
	v_mov_b32_e32 v77, v4
	v_mov_b32_e32 v78, v4
	v_mov_b32_e32 v79, v4
	v_mov_b32_e32 v84, v4
	v_mov_b32_e32 v85, v4
	v_mov_b32_e32 v86, v4
	v_mov_b32_e32 v87, v4
	v_mov_b32_e32 v92, v4
	v_mov_b32_e32 v93, v4
	v_mov_b32_e32 v94, v4
	v_mov_b32_e32 v95, v4
	v_mov_b32_e32 v100, v4
	v_mov_b32_e32 v101, v4
	v_mov_b32_e32 v102, v4
	v_mov_b32_e32 v103, v4
	v_mov_b32_e32 v108, v4
	v_mov_b32_e32 v109, v4
	v_mov_b32_e32 v110, v4
	v_mov_b32_e32 v111, v4
	v_mov_b32_e32 v116, v4
	v_mov_b32_e32 v117, v4
	v_mov_b32_e32 v118, v4
	v_mov_b32_e32 v119, v4
	v_mov_b32_e32 v124, v4
	v_mov_b32_e32 v125, v4
	v_mov_b32_e32 v126, v4
	v_mov_b32_e32 v127, v4
	v_mov_b32_e32 v128, v4
	v_mov_b32_e32 v129, v4
	v_mov_b32_e32 v130, v4
	v_mov_b32_e32 v131, v4
	s_barrier

.LBB0_1192:
	s_add_u32 s8, s10, 0x2b800000
	s_addc_u32 s9, s11, 0
	v_bfe_u32 v157, v18, 4, 2
	s_add_u32 s10, s10, 0x200000
	v_and_b32_e32 v1, 15, v18
	v_lshlrev_b32_e32 v19, 4, v157
	v_lshlrev_b32_e32 v18, 2, v18
	s_addc_u32 s11, s11, 0
	s_and_b32 s13, s13, 3
	s_lshl_b32 s55, s5, 6
	v_lshl_or_b32 v19, v1, 6, v19
	s_lshl_b32 s5, s5, 13
	v_and_b32_e32 v18, 32, v18
	s_add_i32 m0, s50, 0x18000
	v_lshl_add_u64 v[10:11], v[10:11], 0, s[86:87]
	v_bitop3_b32 v20, v19, s5, v18 bitop3:0xde
	s_lshl_b32 s61, s13, 5
	s_lshl_b32 s5, s13, 12
	global_load_lds_dwordx4 v[10:11], off
	v_lshl_add_u64 v[8:9], v[8:9], 0, s[86:87]
	s_add_i32 m0, s50, 0x1a000
	s_add_i32 s76, s50, 0x8000
	s_add_i32 s77, s50, 0xa000
	global_load_lds_dwordx4 v[8:9], off
	v_lshl_add_u64 v[4:5], v[4:5], 0, s[86:87]
	s_mov_b32 m0, s76
	s_add_u32 s14, s24, 0x100080
	global_load_lds_dwordx4 v[4:5], off
	v_lshl_add_u64 v[4:5], v[6:7], 0, s[86:87]
	s_mov_b32 m0, s77
	s_addc_u32 s15, s25, 0
	global_load_lds_dwordx4 v[4:5], off
	s_add_i32 m0, s50, 0x1c000
	v_lshl_add_u64 v[4:5], s[14:15], 0, v[2:3]
	global_load_lds_dwordx4 v[4:5], off
	v_lshl_add_u64 v[4:5], s[14:15], 0, v[132:133]
	s_add_i32 m0, s50, 0x1e000
	s_cmpk_lt_u32 s4, 0x100
	global_load_lds_dwordx4 v[4:5], off
	s_waitcnt vmcnt(8)
	s_barrier
	v_lshlrev_b32_e32 v4, 16, v15
	v_and_b32_e32 v4, 0xfffe0000, v4
	v_lshl_add_u32 v4, v16, 13, v4
	v_and_b32_e32 v5, 1, v15
	v_lshl_or_b32 v4, v5, 6, v4
	v_bitop3_b32 v163, v19, s5, v18 bitop3:0xde
	s_cselect_b64 s[14:15], -1, 0
	s_and_b32 s4, s4, 0xffffff00
	s_lshl_b32 s5, s13, 6
	v_lshl_add_u32 v134, v17, 1, v4
	v_lshlrev_b32_e32 v4, 16, v12
	s_or_b32 s78, s5, s4
	s_lshl_b32 s4, s13, 2
	v_and_b32_e32 v4, 0xfffe0000, v4
	s_waitcnt vmcnt(6)
	s_add_i32 s88, s4, 0
	v_lshl_add_u32 v4, v13, 13, v4
	v_and_b32_e32 v5, 1, v12
	v_readlane_b32 s4, v254, 24
	v_lshl_or_b32 v4, v5, 6, v4
	s_mov_b32 s16, s4
	v_readlane_b32 s4, v254, 31
	s_ashr_i32 s85, s22, 31
	s_add_i32 s88, s88, 0x20400
	v_mov_b32_e32 v135, v3
	v_lshl_add_u32 v136, v14, 1, v4
	v_mov_b32_e32 v137, v3
	s_mov_b32 s93, 0
	v_add_u32_e32 v186, 0, v20
	s_mov_b32 s17, s4
	s_barrier
	v_readlane_b32 s5, v254, 32
	s_branch .LBB0_1195
